# GEMM phase prologues: K-tile 1's staging loads issued before the first wait (vmcnt(2) -> vmcnt(8) after them), so the two prologue load groups overlap instead of two serial round trips; on top of the
# speedup vs baseline: 1.0018x; 1.0017x over previous
; #define PG8_STAGE(bufoff, gbase, voff) do { _Pragma("unroll") for (int _i = 0; _i < 2; ++_i) \
;         __builtin_amdgcn_global_load_lds((const unsigned*)((const char*)(gbase) + _i * voff##_step + (voff)), (PG8_LAS unsigned*)(lds + (bufoff) + ldsw + _i * 8192), 16, 0, 0); } while (0)
; #define PG8_WAIT_V(n) asm volatile("s_waitcnt vmcnt(" #n ")" ::: "memory")
; #define PG8_BAR __builtin_amdgcn_s_barrier()
; template <class Epi, class Sched, bool ALIGN_EPI = false, bool SP2 = false>
; __device__ __forceinline__ void gemm_phase(PG8_LAS unsigned char* lds, const Gemm g, const Sched& S, const Epi& E) {
;     ...
;     const char* cA = (const char*)S.opA(g, cur) + (size_t)cur.pm * tstepA; const char* cB = (const char*)S.opB(g, cur) + (size_t)cur.pn * tstepB;
;     S.a_ready(cur);
;     if constexpr (SP2) {
;         PG8_STAGE(PG8_SB(0, 0), cB, voffB); PG8_STAGE(PG8_SB(0, 1), cB + hstepB, voffB); PG8_STAGE(PG8_SA(0, 0), cA, voffA); PG8_STAGE(PG8_SA(0, 1), cA + hstepA, voffA);
;         if (wr == 1) PG8_BAR;
;         PG8_WAIT_V(2); PG8_BAR;
;         PG8_STAGE(PG8_SB(1, 0), cB + kstep, voffB); PG8_STAGE(PG8_SA(1, 0), cA + kstep, voffA); PG8_STAGE(PG8_SB(1, 1), cB + hstepB + kstep, voffB);
;         if (Epi::NST > 0) PG8_WAIT_V(0); else PG8_WAIT_V(6);
;         PG8_BAR;
.LBB0_122:
	s_lshl_b32 s0, s26, 21
	s_add_i32 s0, s0, s14
	s_lshl_b64 s[6:7], s[0:1], 2
	v_readlane_b32 s0, v253, 2
	s_add_u32 s8, s0, s6
	v_readlane_b32 s0, v253, 3
	s_addc_u32 s9, s0, s7
	v_lshl_add_u64 v[12:13], v[4:5], 0, s[78:79]
	s_add_i32 m0, s37, 0x18000
	s_nop 0
	global_load_lds_dwordx4 v[12:13], off
	v_lshl_add_u64 v[12:13], v[4:5], 0, s[84:85]
	s_add_i32 m0, s37, 0x1a000
	s_add_i32 s0, s37, 0x8000
	global_load_lds_dwordx4 v[12:13], off
	v_lshl_add_u64 v[12:13], v[6:7], 0, s[78:79]
	s_mov_b32 m0, s0
	s_add_i32 s41, s37, 0xa000
	global_load_lds_dwordx4 v[12:13], off
	v_lshl_add_u64 v[6:7], v[6:7], 0, s[92:93]
	s_mov_b32 m0, s41
	s_and_b32 s4, s4, 3
	global_load_lds_dwordx4 v[6:7], off
	v_lshl_add_u64 v[6:7], v[4:5], 0, s[10:11]
	s_add_i32 m0, s37, 0x1c000
	v_lshl_add_u64 v[4:5], v[4:5], 0, s[20:21]
	global_load_lds_dwordx4 v[6:7], off
	s_add_i32 m0, s37, 0x1e000
	s_lshl_b32 s5, s3, 13
	global_load_lds_dwordx4 v[4:5], off
	s_waitcnt vmcnt(8)
	s_barrier
	v_bfe_u32 v5, v3, 4, 2
	v_and_b32_e32 v4, 15, v3
	v_lshlrev_b32_e32 v7, 4, v5
	v_lshl_or_b32 v3, s3, 6, v4
	v_lshl_or_b32 v7, v4, 6, v7
	v_lshlrev_b32_e32 v4, 2, v4
	v_and_b32_e32 v12, 32, v4
	v_bitop3_b32 v13, v7, s5, v12 bitop3:0xde
	s_lshl_b32 s5, s4, 12
	s_cmpk_lt_u32 s2, 0x100
	s_cselect_b64 s[20:21], -1, 0
	s_lshl_b32 s2, s3, 11
	s_lshl_b32 s3, s4, 9
	s_add_i32 s2, s2, 0
	s_add_i32 s2, s2, s3
	s_add_i32 s2, s2, 0x20400
	v_lshlrev_b32_e32 v6, 3, v5
	v_cmp_eq_u32_e64 s[6:7], 0, v5
	v_add_u32_e32 v161, s2, v4
	v_lshlrev_b32_e32 v4, 5, v5
	v_mov_b32_e32 v5, v2
	s_movk_i32 s2, 0x840
	v_lshl_add_u64 v[136:137], s[8:9], 0, v[4:5]
	v_lshrrev_b32_e32 v5, 1, v9
	v_mul_lo_u32 v4, v8, s2
	s_mov_b32 s2, 0x8400
	s_waitcnt vmcnt(0)
	v_mad_u64_u32 v[4:5], s[2:3], v5, s2, v[4:5]
	v_or_b32_e32 v4, v4, v10
	v_readlane_b32 s30, v254, 14
	v_bitop3_b32 v160, v7, s5, v12 bitop3:0xde
	s_mov_b32 s42, 0
	v_lshl_or_b32 v162, s4, 5, v6
	v_add_lshl_u32 v138, v4, v11, 1
	v_mov_b32_e32 v139, v2
	s_mov_b32 s3, -1
	v_add_u32_e32 v163, 0, v13
	v_readlane_b32 s2, v254, 8
	v_readlane_b32 s43, v254, 13
	v_readlane_b32 s31, v254, 15
	s_barrier
	s_branch .LBB0_125

; #define PG8_STAGE(bufoff, gbase, voff) do { _Pragma("unroll") for (int _i = 0; _i < 2; ++_i) \
;         __builtin_amdgcn_global_load_lds((const unsigned*)((const char*)(gbase) + _i * voff##_step + (voff)), (PG8_LAS unsigned*)(lds + (bufoff) + ldsw + _i * 8192), 16, 0, 0); } while (0)
; #define PG8_WAIT_V(n) asm volatile("s_waitcnt vmcnt(" #n ")" ::: "memory")
; #define PG8_BAR __builtin_amdgcn_s_barrier()
; template <class Epi, class Sched, bool ALIGN_EPI = false, bool SP2 = false>
; __device__ __forceinline__ void gemm_phase(PG8_LAS unsigned char* lds, const Gemm g, const Sched& S, const Epi& E) {
;     ...
;     const char* cA = (const char*)S.opA(g, cur) + (size_t)cur.pm * tstepA; const char* cB = (const char*)S.opB(g, cur) + (size_t)cur.pn * tstepB;
;     S.a_ready(cur);
;     if constexpr (SP2) {
;         PG8_STAGE(PG8_SB(0, 0), cB, voffB); PG8_STAGE(PG8_SB(0, 1), cB + hstepB, voffB); PG8_STAGE(PG8_SA(0, 0), cA, voffA); PG8_STAGE(PG8_SA(0, 1), cA + hstepA, voffA);
;         if (wr == 1) PG8_BAR;
;         PG8_WAIT_V(2); PG8_BAR;
;         PG8_STAGE(PG8_SB(1, 0), cB + kstep, voffB); PG8_STAGE(PG8_SA(1, 0), cA + kstep, voffA); PG8_STAGE(PG8_SB(1, 1), cB + hstepB + kstep, voffB);
;         if (Epi::NST > 0) PG8_WAIT_V(0); else PG8_WAIT_V(6);
;         PG8_BAR;
.LBB0_218:
	v_readlane_b32 s8, v255, 47
	s_mul_i32 s0, s8, 3
	s_add_i32 s15, s15, s0
	v_readlane_b32 s9, v255, 48
	s_lshl_b32 s0, s15, 20
	s_lshl_b64 s[8:9], s[0:1], 2
	v_readlane_b32 s0, v253, 2
	v_bfe_u32 v3, v12, 4, 2
	s_add_u32 s16, s0, s8
	v_readlane_b32 s0, v253, 3
	v_and_b32_e32 v13, 15, v12
	v_lshlrev_b32_e32 v175, 4, v3
	v_lshlrev_b32_e32 v12, 2, v12
	s_addc_u32 s17, s0, s9
	s_and_b32 s15, s5, 3
	v_lshl_or_b32 v174, s4, 6, v13
	v_lshl_or_b32 v13, v13, 6, v175
	s_lshl_b32 s0, s4, 13
	v_and_b32_e32 v12, 32, v12
	v_bitop3_b32 v15, v13, s0, v12 bitop3:0xde
	s_lshl_b32 s0, s15, 12
	v_bitop3_b32 v176, v13, s0, v12 bitop3:0xde
	v_lshl_add_u64 v[12:13], v[4:5], 0, s[78:79]
	s_add_i32 m0, s31, 0x18000
	s_mov_b64 s[4:5], 0xb0080
	global_load_lds_dwordx4 v[12:13], off
	v_lshl_add_u64 v[12:13], v[4:5], 0, s[4:5]
	s_add_i32 m0, s31, 0x1a000
	s_add_i32 s37, s31, 0x8000
	global_load_lds_dwordx4 v[12:13], off
	v_lshl_add_u64 v[12:13], v[6:7], 0, s[78:79]
	s_mov_b32 m0, s37
	s_add_i32 s38, s31, 0xa000
	global_load_lds_dwordx4 v[12:13], off
	v_lshl_add_u64 v[6:7], v[6:7], 0, s[4:5]
	s_mov_b32 m0, s38
	s_mov_b64 s[4:5], 0x160080
	global_load_lds_dwordx4 v[6:7], off
	v_lshl_add_u64 v[6:7], v[4:5], 0, s[4:5]
	s_add_i32 m0, s31, 0x1c000
	s_mov_b64 s[4:5], 0x210080
	global_load_lds_dwordx4 v[6:7], off
	v_lshl_add_u64 v[4:5], v[4:5], 0, s[4:5]
	s_add_i32 m0, s31, 0x1e000
	s_movk_i32 s0, 0x1600
	global_load_lds_dwordx4 v[4:5], off
	s_waitcnt vmcnt(8)
	s_barrier
	v_lshrrev_b32_e32 v5, 1, v8
	v_mul_lo_u32 v4, v10, s0
	s_mov_b32 s0, 0x16000
	s_waitcnt vmcnt(0)
	v_mad_u64_u32 v[4:5], s[4:5], v5, s0, v[4:5]
	v_lshlrev_b32_e32 v14, 3, v3
	s_cmpk_lt_u32 s6, 0x100
	v_or_b32_e32 v4, v4, v9
	v_lshl_or_b32 v177, s15, 5, v14
	s_cselect_b64 s[18:19], -1, 0
	v_cmp_eq_u32_e64 s[6:7], 2, v3
	v_add_lshl_u32 v164, v4, v11, 1
	v_mov_b32_e32 v165, v2
	s_mov_b32 s0, 0
	v_add_u32_e32 v178, 0, v15
	s_barrier
	s_branch .LBB0_221

; #define PG8_STAGE(bufoff, gbase, voff) do { _Pragma("unroll") for (int _i = 0; _i < 2; ++_i) \
;         __builtin_amdgcn_global_load_lds((const unsigned*)((const char*)(gbase) + _i * voff##_step + (voff)), (PG8_LAS unsigned*)(lds + (bufoff) + ldsw + _i * 8192), 16, 0, 0); } while (0)
; #define PG8_WAIT_V(n) asm volatile("s_waitcnt vmcnt(" #n ")" ::: "memory")
; #define PG8_BAR __builtin_amdgcn_s_barrier()
; template <class Epi, class Sched, bool ALIGN_EPI = false, bool SP2 = false>
; __device__ __forceinline__ void gemm_phase(PG8_LAS unsigned char* lds, const Gemm g, const Sched& S, const Epi& E) {
;     ...
;     const char* cA = (const char*)S.opA(g, cur) + (size_t)cur.pm * tstepA; const char* cB = (const char*)S.opB(g, cur) + (size_t)cur.pn * tstepB;
;     S.a_ready(cur);
;     if constexpr (SP2) {
;         PG8_STAGE(PG8_SB(0, 0), cB, voffB); PG8_STAGE(PG8_SB(0, 1), cB + hstepB, voffB); PG8_STAGE(PG8_SA(0, 0), cA, voffA); PG8_STAGE(PG8_SA(0, 1), cA + hstepA, voffA);
;         if (wr == 1) PG8_BAR;
;         PG8_WAIT_V(2); PG8_BAR;
;         PG8_STAGE(PG8_SB(1, 0), cB + kstep, voffB); PG8_STAGE(PG8_SA(1, 0), cA + kstep, voffA); PG8_STAGE(PG8_SB(1, 1), cB + hstepB + kstep, voffB);
;         if (Epi::NST > 0) PG8_WAIT_V(0); else PG8_WAIT_V(6);
;         PG8_BAR;
.LBB0_312:
	v_readlane_b32 s6, v255, 47
	v_readlane_b32 s7, v255, 48
	v_readlane_b32 s36, v252, 22
	s_lshl_b64 s[6:7], s[6:7], 14
	v_readlane_b32 s50, v252, 36
	v_readlane_b32 s37, v252, 23
	v_readlane_b32 s51, v252, 37
	s_add_u32 s36, s50, s6
	v_readlane_b32 s38, v252, 24
	s_addc_u32 s37, s51, s7
	v_lshl_add_u64 v[12:13], v[4:5], 0, s[78:79]
	s_add_i32 m0, s30, 0x18000
	v_readlane_b32 s39, v252, 25
	global_load_lds_dwordx4 v[12:13], off
	v_lshl_add_u64 v[4:5], v[4:5], 0, s[84:85]
	s_add_i32 m0, s30, 0x1a000
	s_add_i32 s38, s30, 0x8000
	global_load_lds_dwordx4 v[4:5], off
	v_lshl_add_u64 v[4:5], v[6:7], 0, s[78:79]
	s_mov_b32 m0, s38
	s_add_i32 s39, s30, 0xa000
	v_readlane_b32 s6, v254, 31
	global_load_lds_dwordx4 v[4:5], off
	v_lshl_add_u64 v[4:5], v[6:7], 0, s[92:93]
	s_mov_b32 m0, s39
	v_readlane_b32 s7, v254, 32
	global_load_lds_dwordx4 v[4:5], off
	s_nop 0
	v_lshl_add_u64 v[4:5], s[6:7], 0, v[164:165]
	s_add_i32 m0, s30, 0x1c000
	s_and_b32 s3, s3, 3
	global_load_lds_dwordx4 v[4:5], off
	v_lshl_add_u64 v[4:5], v[4:5], 0, s[90:91]
	s_add_i32 m0, s30, 0x1e000
	s_lshl_b32 s5, s4, 13
	global_load_lds_dwordx4 v[4:5], off
	s_waitcnt vmcnt(8)
	s_barrier
	v_and_b32_e32 v4, 15, v3
	v_bfe_u32 v3, v3, 4, 2
	v_lshlrev_b32_e32 v6, 4, v3
	v_lshl_or_b32 v196, s4, 6, v4
	v_lshl_or_b32 v6, v4, 6, v6
	v_lshlrev_b32_e32 v4, 2, v4
	v_and_b32_e32 v7, 32, v4
	v_bitop3_b32 v12, v6, s5, v7 bitop3:0xde
	s_lshl_b32 s5, s3, 12
	v_readlane_b32 s41, v252, 27
	v_lshlrev_b32_e32 v5, 3, v3
	s_cmpk_lt_u32 s2, 0x100
	s_cselect_b64 s[18:19], -1, 0
	v_lshl_or_b32 v198, s3, 5, v5
	s_lshl_b32 s2, s4, 11
	s_lshl_b32 s4, s3, 9
	s_lshl_b32 s41, s3, 6
	s_lshl_b32 s3, s3, 3
	v_readlane_b32 s8, v254, 2
	v_readlane_b32 s9, v254, 3
	s_add_u32 s20, s8, s3
	s_addc_u32 s21, s9, 0
	s_add_i32 s2, s2, 0
	s_add_i32 s2, s2, s4
	s_add_i32 s2, s2, 0x20400
	v_add_u32_e32 v199, s2, v4
	v_readlane_b32 s2, v255, 51
	v_lshlrev_b32_e32 v4, 5, v3
	v_mov_b32_e32 v5, v2
	v_readlane_b32 s3, v255, 52
	s_waitcnt vmcnt(0)
	v_readlane_b32 s40, v252, 26
	v_readlane_b32 s43, v252, 29
	v_lshl_add_u64 v[4:5], s[2:3], 0, v[4:5]
	s_mov_b64 s[2:3], 0x400000
	v_lshl_add_u64 v[168:169], v[4:5], 0, s[2:3]
	v_readlane_b32 s2, v253, 0
	v_lshlrev_b32_e32 v4, 2, v198
	v_mov_b32_e32 v5, v2
	v_readlane_b32 s3, v253, 1
	v_readlane_b32 s44, v252, 30
	v_readlane_b32 s12, v254, 29
	v_lshl_add_u64 v[170:171], s[2:3], 0, v[4:5]
	s_movk_i32 s2, 0x840
	v_lshrrev_b32_e32 v5, 1, v9
	v_mul_lo_u32 v4, v8, s2
	s_mov_b32 s2, 0x8400
	v_mad_u64_u32 v[4:5], s[2:3], v5, s2, v[4:5]
	v_or_b32_e32 v4, v4, v10
	v_readlane_b32 s14, v254, 25
	v_readlane_b32 s42, v252, 28
	v_bitop3_b32 v197, v6, s5, v7 bitop3:0xde
	s_mov_b32 s40, 0
	v_cmp_eq_u32_e64 s[6:7], 0, v3
	v_add_lshl_u32 v172, v4, v11, 1
	v_mov_b32_e32 v173, v2
	s_mov_b32 s43, -1
	v_add_u32_e32 v200, 0, v12
	v_readlane_b32 s44, v254, 11
	v_readlane_b32 s2, v254, 22
	v_readlane_b32 s13, v254, 30
	v_readlane_b32 s15, v254, 26
	v_readlane_b32 s45, v252, 31
	v_readlane_b32 s46, v252, 32
	v_readlane_b32 s47, v252, 33
	v_readlane_b32 s48, v252, 34
	v_readlane_b32 s49, v252, 35
	s_barrier
	s_branch .LBB0_315

; #define PG8_STAGE(bufoff, gbase, voff) do { _Pragma("unroll") for (int _i = 0; _i < 2; ++_i) \
;         __builtin_amdgcn_global_load_lds((const unsigned*)((const char*)(gbase) + _i * voff##_step + (voff)), (PG8_LAS unsigned*)(lds + (bufoff) + ldsw + _i * 8192), 16, 0, 0); } while (0)
; #define PG8_WAIT_V(n) asm volatile("s_waitcnt vmcnt(" #n ")" ::: "memory")
; #define PG8_BAR __builtin_amdgcn_s_barrier()
; template <class Epi, class Sched, bool ALIGN_EPI = false, bool SP2 = false>
; __device__ __forceinline__ void gemm_phase(PG8_LAS unsigned char* lds, const Gemm g, const Sched& S, const Epi& E) {
;     ...
;     const char* cA = (const char*)S.opA(g, cur) + (size_t)cur.pm * tstepA; const char* cB = (const char*)S.opB(g, cur) + (size_t)cur.pn * tstepB;
;     S.a_ready(cur);
;     if constexpr (SP2) {
;         PG8_STAGE(PG8_SB(0, 0), cB, voffB); PG8_STAGE(PG8_SB(0, 1), cB + hstepB, voffB); PG8_STAGE(PG8_SA(0, 0), cA, voffA); PG8_STAGE(PG8_SA(0, 1), cA + hstepA, voffA);
;         if (wr == 1) PG8_BAR;
;         PG8_WAIT_V(2); PG8_BAR;
;         PG8_STAGE(PG8_SB(1, 0), cB + kstep, voffB); PG8_STAGE(PG8_SA(1, 0), cA + kstep, voffA); PG8_STAGE(PG8_SB(1, 1), cB + hstepB + kstep, voffB);
;         if (Epi::NST > 0) PG8_WAIT_V(0); else PG8_WAIT_V(6);
;         PG8_BAR;
.LBB0_688:
	v_readlane_b32 s4, v255, 51
	v_bfe_u32 v3, v12, 4, 2
	v_readlane_b32 s5, v255, 52
	s_add_u32 s14, s4, 0x800000
	v_and_b32_e32 v13, 15, v12
	v_lshlrev_b32_e32 v175, 4, v3
	v_lshlrev_b32_e32 v12, 2, v12
	s_addc_u32 s15, s5, 0
	s_and_b32 s35, s2, 3
	v_lshl_or_b32 v174, s3, 6, v13
	v_lshl_or_b32 v13, v13, 6, v175
	s_lshl_b32 s2, s3, 13
	v_and_b32_e32 v12, 32, v12
	v_bitop3_b32 v15, v13, s2, v12 bitop3:0xde
	s_lshl_b32 s2, s35, 12
	v_bitop3_b32 v176, v13, s2, v12 bitop3:0xde
	v_lshl_add_u64 v[12:13], v[4:5], 0, s[78:79]
	s_add_i32 m0, s29, 0x18000
	s_nop 0
	global_load_lds_dwordx4 v[12:13], off
	v_lshl_add_u64 v[4:5], v[4:5], 0, s[84:85]
	s_add_i32 m0, s29, 0x1a000
	s_add_i32 s36, s29, 0x8000
	global_load_lds_dwordx4 v[4:5], off
	v_lshl_add_u64 v[4:5], v[6:7], 0, s[78:79]
	s_mov_b32 m0, s36
	s_add_i32 s37, s29, 0xa000
	v_readlane_b32 s2, v254, 44
	global_load_lds_dwordx4 v[4:5], off
	v_lshl_add_u64 v[4:5], v[6:7], 0, s[92:93]
	s_mov_b32 m0, s37
	v_readlane_b32 s3, v254, 45
	global_load_lds_dwordx4 v[4:5], off
	s_nop 0
	v_lshl_add_u64 v[4:5], s[2:3], 0, v[160:161]
	s_add_i32 m0, s29, 0x1c000
	v_lshlrev_b32_e32 v14, 3, v3
	global_load_lds_dwordx4 v[4:5], off
	v_lshl_add_u64 v[4:5], v[4:5], 0, s[90:91]
	s_add_i32 m0, s29, 0x1e000
	s_cmpk_lt_u32 s0, 0x100
	global_load_lds_dwordx4 v[4:5], off
	s_waitcnt vmcnt(8)
	s_barrier
	s_movk_i32 s0, 0x840
	v_lshrrev_b32_e32 v5, 1, v9
	v_mul_lo_u32 v4, v8, s0
	s_mov_b32 s0, 0x8400
	s_waitcnt vmcnt(0)
	v_mad_u64_u32 v[4:5], s[2:3], v5, s0, v[4:5]
	v_or_b32_e32 v4, v4, v10
	v_readlane_b32 s24, v254, 42
	v_readlane_b32 s26, v254, 38
	v_lshl_or_b32 v177, s35, 5, v14
	s_cselect_b64 s[16:17], -1, 0
	v_cmp_eq_u32_e64 s[6:7], 2, v3
	v_add_lshl_u32 v164, v4, v11, 1
	v_mov_b32_e32 v165, v2
	s_mov_b32 s38, 0
	v_add_u32_e32 v178, 0, v15
	v_readlane_b32 s0, v254, 12
	v_readlane_b32 s2, v254, 37
	v_readlane_b32 s25, v254, 43
	v_readlane_b32 s27, v254, 39
	s_barrier
	s_branch .LBB0_691
